# v49 + GLA-C chunk start: the two ga row loads of a thread issued together instead of a two-trip load/wait loop
# speedup vs baseline: 1.0221x; 1.0009x over previous
.LBB0_1053:
	s_nop 0
	s_nop 0
	v_and_b32_e32 v3, 64, v68
	v_xor_b32_e32 v2, 32, v68
	v_add_u32_e32 v3, 64, v3
	v_cmp_lt_i32_e32 vcc, v2, v3
	s_mov_b64 s[20:21], -1
	s_mov_b64 s[22:23], -1
	v_cndmask_b32_e32 v2, v68, v2, vcc
	v_lshlrev_b32_e32 v2, 2, v2
	ds_bpermute_b32 v6, v2, v71
	ds_bpermute_b32 v5, v2, v50
	ds_bpermute_b32 v3, v2, v57
	ds_bpermute_b32 v7, v2, v69
	ds_bpermute_b32 v4, v2, v59
	ds_bpermute_b32 v2, v2, v70
	s_waitcnt lgkmcnt(5)
	v_cmp_nlt_f32_e32 vcc, v71, v6
	s_and_saveexec_b64 s[18:19], vcc
	s_cbranch_execz .LBB0_1057
	v_cmp_eq_f32_e32 vcc, v71, v6
	s_mov_b64 s[22:23], 0
	s_and_saveexec_b64 s[24:25], vcc
	s_cbranch_execz .LBB0_1056
	s_waitcnt lgkmcnt(2)
	v_cmp_lt_i32_e32 vcc, v7, v69
	s_and_b64 s[22:23], vcc, exec

.LBB0_1417:
	s_or_b64 exec, exec, s[0:1]
	s_waitcnt lgkmcnt(0)
	s_barrier
	v_mov_b32_e32 v2, s80
	ds_read_b32 v2, v2
	s_waitcnt lgkmcnt(0)
	s_barrier
	s_movk_i32 s0, 0xff
	s_waitcnt lgkmcnt(0)
	v_cmp_lt_i32_e32 vcc, s0, v2
	v_readfirstlane_b32 s74, v2
	s_mov_b64 s[0:1], -1
	s_cbranch_vccnz .LBB0_1412
	v_mov_b32_e32 v2, s81
	v_mov_b32_e32 v3, s82
	ds_read_b32 v2, v2
	ds_read_b32 v3, v3
	v_or_b32_e32 v18, 32, v167
	v_mov_b32_e32 v91, v192
	v_or_b32_e32 v92, 0xfffffe00, v0
	s_waitcnt lgkmcnt(1)
	v_readfirstlane_b32 s0, v2
	s_waitcnt lgkmcnt(0)
	v_readfirstlane_b32 s1, v3
	s_nop 1
	v_lshl_add_u64 v[2:3], v[132:133], 2, s[0:1]
	v_add_co_u32_e32 v12, vcc, s83, v2
	v_lshl_add_u64 v[4:5], v[146:147], 2, s[0:1]
	v_lshl_add_u64 v[6:7], v[136:137], 2, s[0:1]
	v_lshl_add_u64 v[8:9], v[138:139], 2, s[0:1]
	v_lshl_add_u64 v[10:11], v[140:141], 2, s[0:1]
	v_addc_co_u32_e32 v13, vcc, 0, v3, vcc
	flat_load_dword v22, v[2:3]
	flat_load_dword v23, v[4:5] offset:1024
	flat_load_dword v20, v[4:5] offset:2048
	flat_load_dword v21, v[4:5] offset:3072
	flat_load_dword v24, v[6:7]
	flat_load_dword v25, v[8:9]
	flat_load_dword v88, v[10:11]
	flat_load_dword v89, v[12:13] offset:3072
	v_mov_b32_e32 v2, s84
	v_mov_b32_e32 v3, s85
	ds_read_b32 v2, v2
	ds_read_b32 v3, v3
	s_lshl_b32 s0, s74, 6
	v_or_b32_e32 v160, s0, v18
	v_or_b32_e32 v18, 48, v167
	s_waitcnt lgkmcnt(0)
	v_readfirstlane_b32 s1, v2
	v_readfirstlane_b32 s33, v3
	v_or_b32_e32 v156, s0, v18
	v_lshrrev_b32_e32 v18, 5, v0
	v_mov_b32_e32 v2, s1
	v_mov_b32_e32 v3, s33
	v_or_b32_e32 v170, s0, v167
	v_or_b32_e32 v164, s0, v173
	v_or_b32_e32 v18, s0, v18
	v_lshl_add_u64 v[2:3], v[130:131], 2, v[2:3]
	v_mad_i64_i32 v[74:75], s[76:77], v170, s92, v[148:149]
	v_or_b32_e32 v168, s0, v172
	v_mad_i64_i32 v[78:79], s[76:77], v164, s92, v[148:149]
	v_or_b32_e32 v162, s0, v174
	v_mad_i64_i32 v[82:83], s[76:77], v160, s92, v[148:149]
	v_or_b32_e32 v158, s0, v176
	v_mad_i64_i32 v[86:87], s[76:77], v156, s92, v[148:149]
	v_or_b32_e32 v154, s0, v178
	v_mad_i64_i32 v[18:19], s[76:77], v18, s92, v[150:151]
	flat_load_dword v90, v[2:3]
	v_mad_i64_i32 v[76:77], s[76:77], v168, s92, v[148:149]
	global_load_dwordx4 v[2:5], v[74:75], off offset:1024
	global_load_dwordx4 v[6:9], v[76:77], off offset:1024
	v_mad_i64_i32 v[80:81], s[76:77], v162, s92, v[148:149]
	global_load_dwordx4 v[10:13], v[78:79], off offset:1024
	global_load_dwordx4 v[14:17], v[80:81], off offset:1024
	v_mad_i64_i32 v[84:85], s[76:77], v158, s92, v[148:149]
	global_load_dwordx4 v[26:29], v[82:83], off offset:1024
	global_load_dwordx4 v[30:33], v[84:85], off offset:1024
	v_mad_i64_i32 v[114:115], s[76:77], v154, s92, v[148:149]
	global_load_dwordx4 v[34:37], v[86:87], off offset:1024
	global_load_dwordx4 v[38:41], v[114:115], off offset:1024
	global_load_dwordx4 v[42:45], v[18:19], off
	global_load_dwordx4 v[46:49], v[18:19], off offset:512
	v_or_b32_e32 v18, s0, v180
	v_mad_i64_i32 v[18:19], s[76:77], v18, s92, v[150:151]
	global_load_dwordx4 v[50:53], v[18:19], off
	global_load_dwordx4 v[54:57], v[18:19], off offset:512
	v_or_b32_e32 v18, s0, v181
	v_mad_i64_i32 v[18:19], s[76:77], v18, s92, v[150:151]
	global_load_dwordx4 v[58:61], v[18:19], off
	global_load_dwordx4 v[62:65], v[18:19], off offset:512
	v_or_b32_e32 v18, s0, v182
	v_mad_i64_i32 v[18:19], s[76:77], v18, s92, v[150:151]
	global_load_dwordx4 v[66:69], v[18:19], off
	global_load_dwordx4 v[70:73], v[18:19], off offset:512
	s_ashr_i32 s1, s0, 31
	s_lshl_b64 s[0:1], s[0:1], 6
	v_ashrrev_i32_e32 v171, 31, v170
	v_ashrrev_i32_e32 v169, 31, v168
	v_ashrrev_i32_e32 v165, 31, v164
	v_ashrrev_i32_e32 v163, 31, v162
	v_ashrrev_i32_e32 v161, 31, v160
	v_ashrrev_i32_e32 v159, 31, v158
	v_ashrrev_i32_e32 v157, 31, v156
	v_ashrrev_i32_e32 v155, 31, v154
	v_lshl_add_u64 v[18:19], v[152:153], 0, s[0:1]
	s_mov_b64 s[0:1], 0
	global_load_dword v93, v[18:19], off
	global_load_dword v92, v[18:19], off offset:2048
	s_waitcnt vmcnt(0)
	ds_write_b32 v91, v93
	ds_write_b32 v91, v92 offset:2048
	s_or_b64 exec, exec, s[0:1]
	ds_write_b128 v183, v[42:45] offset:6144
	ds_write_b128 v183, v[46:49] offset:43008
	ds_write_b128 v184, v[50:53] offset:6144
	ds_write_b128 v184, v[54:57] offset:43008
	ds_write_b128 v185, v[58:61] offset:6144
	ds_write_b128 v185, v[62:65] offset:43008
	ds_write_b128 v186, v[66:69] offset:6144
	ds_write_b128 v186, v[70:73] offset:43008
	ds_write_b128 v223, v[2:5]
	ds_write_b128 v224, v[6:9]
	ds_write_b128 v225, v[10:13]
	ds_write_b128 v226, v[14:17]
	ds_write_b128 v227, v[26:29]
	ds_write_b128 v228, v[30:33]
	ds_write_b128 v229, v[34:37]
	ds_write_b128 v230, v[38:41]
	s_waitcnt lgkmcnt(0)
	s_barrier
	v_cvt_pk_bf16_f32 v18, v22, v23
	ds_read_b128 v[26:29], v187
	ds_read_b128 v[30:33], v187 offset:16
	v_lshlrev_b32_e32 v92, 16, v18
	v_and_b32_e32 v93, 0xffff0000, v18
	v_cvt_pk_bf16_f32 v19, v20, v21
	v_pk_add_f32 v[22:23], v[22:23], v[92:93] neg_lo:[0,1] neg_hi:[0,1]
	v_lshlrev_b32_e32 v92, 16, v19
	v_and_b32_e32 v93, 0xffff0000, v19
	v_pk_add_f32 v[20:21], v[20:21], v[92:93] neg_lo:[0,1] neg_hi:[0,1]
	v_cvt_pk_bf16_f32 v22, v22, v23
	v_cvt_pk_bf16_f32 v23, v20, v21
	v_cvt_pk_bf16_f32 v20, v24, v25
	v_lshlrev_b32_e32 v92, 16, v20
	v_and_b32_e32 v93, 0xffff0000, v20
	v_cvt_pk_bf16_f32 v21, v88, v89
	s_waitcnt lgkmcnt(0)
	v_cvt_pk_bf16_f32 v34, v26, v27
	v_cvt_pk_bf16_f32 v35, v28, v29
	v_cvt_pk_bf16_f32 v36, v30, v31
	v_cvt_pk_bf16_f32 v37, v32, v33
	v_pk_add_f32 v[24:25], v[24:25], v[92:93] neg_lo:[0,1] neg_hi:[0,1]
	v_lshlrev_b32_e32 v92, 16, v21
	v_and_b32_e32 v93, 0xffff0000, v21
	v_pk_add_f32 v[2:3], v[88:89], v[92:93] neg_lo:[0,1] neg_hi:[0,1]
	v_cvt_pk_bf16_f32 v24, v24, v25
	v_cvt_pk_bf16_f32 v25, v2, v3
	v_lshlrev_b32_e32 v2, 16, v34
	v_and_b32_e32 v3, 0xffff0000, v34
	v_pk_add_f32 v[2:3], v[26:27], v[2:3] neg_lo:[0,1] neg_hi:[0,1]
	v_lshlrev_b32_e32 v38, 16, v35
	v_cvt_pk_bf16_f32 v26, v2, v3
	v_mfma_f32_32x32x16_bf16 v[2:17], v[34:37], v[18:21], 0
	v_and_b32_e32 v39, 0xffff0000, v35
	v_add_f32_e64 v28, v28, -v38
	v_add_f32_e64 v29, v29, -v39
	ds_read_b128 v[44:47], v187 offset:2048
	ds_read_b128 v[48:51], v187 offset:2064
	v_cvt_pk_bf16_f32 v27, v28, v29
	v_lshlrev_b32_e32 v28, 16, v36
	v_and_b32_e32 v29, 0xffff0000, v36
	v_mfma_f32_32x32x16_bf16 v[2:17], v[34:37], v[22:25], v[2:17]
	v_add_f32_e64 v28, v30, -v28
	v_add_f32_e64 v29, v31, -v29
	v_lshlrev_b32_e32 v30, 16, v37
	v_and_b32_e32 v31, 0xffff0000, v37
	v_add_f32_e64 v30, v32, -v30
	v_add_f32_e64 v31, v33, -v31
	v_cvt_pk_bf16_f32 v28, v28, v29
	v_cvt_pk_bf16_f32 v29, v30, v31
	s_waitcnt lgkmcnt(1)
	v_cvt_pk_bf16_f32 v52, v44, v45
	v_cvt_pk_bf16_f32 v53, v46, v47
	v_mfma_f32_32x32x16_bf16 v[2:17], v[26:29], v[18:21], v[2:17]
	s_waitcnt lgkmcnt(0)
	v_cvt_pk_bf16_f32 v54, v48, v49
	v_cvt_pk_bf16_f32 v55, v50, v51
	v_lshlrev_b32_e32 v56, 16, v53
	v_and_b32_e32 v57, 0xffff0000, v53
	v_pk_add_f32 v[46:47], v[46:47], v[56:57] neg_lo:[0,1] neg_hi:[0,1]
	s_nop 5
	v_add_f32_e32 v2, v90, v2
	v_mul_f32_e64 v26, |v2|, s93
	v_exp_f32_e32 v26, v26
	v_add_f32_e32 v3, v90, v3
	v_mul_f32_e64 v28, |v3|, s93
	v_exp_f32_e32 v28, v28
	v_add_f32_e32 v26, 1.0, v26
	v_cmp_gt_f32_e32 vcc, s94, v26
	v_add_f32_e32 v4, v90, v4
	v_add_f32_e32 v28, 1.0, v28
	v_cndmask_b32_e64 v27, 0, 32, vcc
	v_ldexp_f32 v26, v26, v27
	v_log_f32_e32 v26, v26
	v_min_f32_e32 v2, 0, v2
	v_add_f32_e32 v5, v90, v5
	v_add_f32_e32 v7, v90, v7
	v_mul_f32_e32 v27, 0x3f317217, v26
	v_fma_f32 v27, v26, s95, -v27
	v_fmac_f32_e32 v27, 0x3377d1cf, v26
	v_fmac_f32_e32 v27, 0x3f317217, v26
	v_cmp_lt_f32_e64 s[0:1], |v26|, s96
	s_nop 1
	v_cndmask_b32_e64 v26, v26, v27, s[0:1]
	v_cndmask_b32_e32 v27, 0, v231, vcc
	v_cmp_gt_f32_e32 vcc, s94, v28
	v_sub_f32_e32 v26, v26, v27
	v_mul_f32_e64 v27, |v4|, s93
	v_cndmask_b32_e64 v29, 0, 32, vcc
	v_ldexp_f32 v28, v28, v29
	v_log_f32_e32 v28, v28
	v_exp_f32_e32 v27, v27
	v_sub_f32_e32 v26, v2, v26
	v_min_f32_e32 v2, 0, v3
	v_mul_f32_e32 v3, 0x3f317217, v28
	v_fma_f32 v3, v28, s95, -v3
	v_fmac_f32_e32 v3, 0x3377d1cf, v28
	v_fmac_f32_e32 v3, 0x3f317217, v28
	v_cmp_lt_f32_e64 s[0:1], |v28|, s96
	v_add_f32_e32 v27, 1.0, v27
	v_mul_f32_e64 v29, |v5|, s93
	v_cndmask_b32_e64 v3, v28, v3, s[0:1]
	v_cndmask_b32_e32 v28, 0, v231, vcc
	v_cmp_gt_f32_e32 vcc, s94, v27
	v_sub_f32_e32 v3, v3, v28
	v_exp_f32_e32 v29, v29
	v_cndmask_b32_e64 v28, 0, 32, vcc
	v_ldexp_f32 v27, v27, v28
	v_log_f32_e32 v28, v27
	v_sub_f32_e32 v27, v2, v3
	v_min_f32_e32 v3, 0, v4
	v_add_f32_e32 v29, 1.0, v29
	v_mul_f32_e32 v4, 0x3f317217, v28
	v_fma_f32 v4, v28, s95, -v4
	v_fmac_f32_e32 v4, 0x3377d1cf, v28
	v_fmac_f32_e32 v4, 0x3f317217, v28
	v_cmp_lt_f32_e64 s[0:1], |v28|, s96
	v_mul_f32_e32 v2, 0x3d800000, v27
	v_fmac_f32_e32 v2, 0x3d800000, v26
	v_cndmask_b32_e64 v4, v28, v4, s[0:1]
	v_cndmask_b32_e32 v28, 0, v231, vcc
	v_cmp_gt_f32_e32 vcc, s94, v29
	v_sub_f32_e32 v4, v4, v28
	v_sub_f32_e32 v28, v3, v4
	v_cndmask_b32_e64 v30, 0, 32, vcc
	v_ldexp_f32 v29, v29, v30
	v_log_f32_e32 v29, v29
	v_min_f32_e32 v3, 0, v5
	v_add_f32_e32 v5, v90, v6
	v_mul_f32_e64 v6, |v5|, s93
	v_exp_f32_e32 v6, v6
	v_mul_f32_e32 v4, 0x3f317217, v29
	v_fma_f32 v4, v29, s95, -v4
	v_fmac_f32_e32 v4, 0x3377d1cf, v29
	v_fmac_f32_e32 v4, 0x3f317217, v29
	v_cmp_lt_f32_e64 s[0:1], |v29|, s96
	v_add_f32_e32 v6, 1.0, v6
	v_mul_f32_e64 v30, |v7|, s93
	v_cndmask_b32_e64 v4, v29, v4, s[0:1]
	v_cndmask_b32_e32 v29, 0, v231, vcc
	v_cmp_gt_f32_e32 vcc, s94, v6
	v_sub_f32_e32 v4, v4, v29
	v_exp_f32_e32 v30, v30
	v_cndmask_b32_e64 v29, 0, 32, vcc
	v_ldexp_f32 v6, v6, v29
	v_log_f32_e32 v6, v6
	v_sub_f32_e32 v29, v3, v4
	v_min_f32_e32 v4, 0, v5
	v_add_f32_e32 v30, 1.0, v30
	v_mul_f32_e32 v5, 0x3f317217, v6
	v_fma_f32 v5, v6, s95, -v5
	v_fmac_f32_e32 v5, 0x3377d1cf, v6
	v_fmac_f32_e32 v5, 0x3f317217, v6
	v_cmp_lt_f32_e64 s[0:1], |v6|, s96
	v_mul_f32_e32 v3, 0x3d800000, v29
	v_fmac_f32_e32 v3, 0x3d800000, v28
	v_cndmask_b32_e64 v5, v6, v5, s[0:1]
	v_cndmask_b32_e32 v6, 0, v231, vcc
	v_cmp_gt_f32_e32 vcc, s94, v30
	v_sub_f32_e32 v5, v5, v6
	v_add_f32_e32 v6, v90, v8
	v_cndmask_b32_e64 v31, 0, 32, vcc
	v_ldexp_f32 v30, v30, v31
	v_log_f32_e32 v31, v30
	v_sub_f32_e32 v30, v4, v5
	v_min_f32_e32 v4, 0, v7
	v_mul_f32_e64 v7, |v6|, s93
	v_exp_f32_e32 v7, v7
	v_mul_f32_e32 v5, 0x3f317217, v31
	v_fma_f32 v5, v31, s95, -v5
	v_fmac_f32_e32 v5, 0x3377d1cf, v31
	v_fmac_f32_e32 v5, 0x3f317217, v31
	v_cmp_lt_f32_e64 s[0:1], |v31|, s96
	v_add_f32_e32 v7, 1.0, v7
	v_cndmask_b32_e32 v8, 0, v231, vcc
	v_cndmask_b32_e64 v5, v31, v5, s[0:1]
	v_cmp_gt_f32_e32 vcc, s94, v7
	v_sub_f32_e32 v5, v5, v8
	v_sub_f32_e32 v31, v4, v5
	v_cndmask_b32_e64 v8, 0, 32, vcc
	v_ldexp_f32 v7, v7, v8
	v_log_f32_e32 v7, v7
	v_min_f32_e32 v4, 0, v6
	v_add_f32_e32 v6, v90, v9
	v_mul_f32_e64 v8, |v6|, s93
	v_exp_f32_e32 v8, v8
	v_mul_f32_e32 v5, 0x3f317217, v7
	v_fma_f32 v5, v7, s95, -v5
	v_fmac_f32_e32 v5, 0x3377d1cf, v7
	v_fmac_f32_e32 v5, 0x3f317217, v7
	v_cmp_lt_f32_e64 s[0:1], |v7|, s96
	v_add_f32_e32 v8, 1.0, v8
	v_add_f32_e32 v42, v2, v3
	v_cndmask_b32_e64 v5, v7, v5, s[0:1]
	v_cndmask_b32_e32 v7, 0, v231, vcc
	v_cmp_gt_f32_e32 vcc, s94, v8
	v_sub_f32_e32 v5, v5, v7
	v_sub_f32_e32 v32, v4, v5
	v_cndmask_b32_e64 v9, 0, 32, vcc
	v_ldexp_f32 v8, v8, v9
	v_log_f32_e32 v8, v8
	v_min_f32_e32 v4, 0, v6
	v_add_f32_e32 v6, v90, v10
	v_mul_f32_e64 v7, |v6|, s93
	v_exp_f32_e32 v7, v7
	v_mul_f32_e32 v5, 0x3f317217, v8
	v_fma_f32 v5, v8, s95, -v5
	v_fmac_f32_e32 v5, 0x3377d1cf, v8
	v_fmac_f32_e32 v5, 0x3f317217, v8
	v_cmp_lt_f32_e64 s[0:1], |v8|, s96
	v_add_f32_e32 v7, 1.0, v7
	v_lshlrev_b32_e32 v2, 16, v52
	v_cndmask_b32_e64 v5, v8, v5, s[0:1]
	v_cndmask_b32_e32 v8, 0, v231, vcc
	v_cmp_gt_f32_e32 vcc, s94, v7
	v_sub_f32_e32 v5, v5, v8
	v_sub_f32_e32 v33, v4, v5
	v_cndmask_b32_e64 v8, 0, 32, vcc
	v_ldexp_f32 v7, v7, v8
	v_log_f32_e32 v7, v7
	v_min_f32_e32 v4, 0, v6
	v_add_f32_e32 v6, v90, v11
	v_mul_f32_e64 v8, |v6|, s93
	v_exp_f32_e32 v8, v8
	v_mul_f32_e32 v5, 0x3f317217, v7
	v_fma_f32 v5, v7, s95, -v5
	v_fmac_f32_e32 v5, 0x3377d1cf, v7
	v_fmac_f32_e32 v5, 0x3f317217, v7
	v_cmp_lt_f32_e64 s[0:1], |v7|, s96
	v_add_f32_e32 v8, 1.0, v8
	v_and_b32_e32 v3, 0xffff0000, v52
	v_cndmask_b32_e64 v5, v7, v5, s[0:1]
	v_cndmask_b32_e32 v7, 0, v231, vcc
	v_cmp_gt_f32_e32 vcc, s94, v8
	v_sub_f32_e32 v5, v5, v7
	v_sub_f32_e32 v34, v4, v5
	v_cndmask_b32_e64 v9, 0, 32, vcc
	v_ldexp_f32 v8, v8, v9
	v_log_f32_e32 v8, v8
	v_min_f32_e32 v4, 0, v6
	v_add_f32_e32 v6, v90, v12
	v_mul_f32_e64 v7, |v6|, s93
	v_exp_f32_e32 v7, v7
	v_mul_f32_e32 v5, 0x3f317217, v8
	v_fma_f32 v5, v8, s95, -v5
	v_fmac_f32_e32 v5, 0x3377d1cf, v8
	v_fmac_f32_e32 v5, 0x3f317217, v8
	v_cmp_lt_f32_e64 s[0:1], |v8|, s96
	v_add_f32_e32 v7, 1.0, v7
	v_pk_add_f32 v[2:3], v[44:45], v[2:3] neg_lo:[0,1] neg_hi:[0,1]
	v_cndmask_b32_e64 v5, v8, v5, s[0:1]
	v_cndmask_b32_e32 v8, 0, v231, vcc
	v_cmp_gt_f32_e32 vcc, s94, v7
	v_sub_f32_e32 v5, v5, v8
	v_sub_f32_e32 v35, v4, v5
	v_cndmask_b32_e64 v8, 0, 32, vcc
	v_ldexp_f32 v7, v7, v8
	v_log_f32_e32 v7, v7
	v_min_f32_e32 v4, 0, v6
	v_add_f32_e32 v6, v90, v13
	v_mul_f32_e64 v8, |v6|, s93
	v_exp_f32_e32 v8, v8
	v_mul_f32_e32 v5, 0x3f317217, v7
	v_fma_f32 v5, v7, s95, -v5
	v_fmac_f32_e32 v5, 0x3377d1cf, v7
	v_fmac_f32_e32 v5, 0x3f317217, v7
	v_cmp_lt_f32_e64 s[0:1], |v7|, s96
	v_add_f32_e32 v8, 1.0, v8
	v_cvt_pk_bf16_f32 v44, v2, v3
	v_cndmask_b32_e64 v5, v7, v5, s[0:1]
	v_cndmask_b32_e32 v7, 0, v231, vcc
	v_cmp_gt_f32_e32 vcc, s94, v8
	v_sub_f32_e32 v5, v5, v7
	v_sub_f32_e32 v36, v4, v5
	v_cndmask_b32_e64 v9, 0, 32, vcc
	v_ldexp_f32 v8, v8, v9
	v_log_f32_e32 v8, v8
	v_min_f32_e32 v4, 0, v6
	v_add_f32_e32 v6, v90, v14
	v_mul_f32_e64 v7, |v6|, s93
	v_exp_f32_e32 v7, v7
	v_mul_f32_e32 v5, 0x3f317217, v8
	v_fma_f32 v5, v8, s95, -v5
	v_fmac_f32_e32 v5, 0x3377d1cf, v8
	v_fmac_f32_e32 v5, 0x3f317217, v8
	v_cmp_lt_f32_e64 s[0:1], |v8|, s96
	v_add_f32_e32 v7, 1.0, v7
	v_cvt_pk_bf16_f32 v45, v46, v47
	v_cndmask_b32_e64 v5, v8, v5, s[0:1]
	v_cndmask_b32_e32 v8, 0, v231, vcc
	v_cmp_gt_f32_e32 vcc, s94, v7
	v_sub_f32_e32 v5, v5, v8
	v_sub_f32_e32 v37, v4, v5
	v_cndmask_b32_e64 v8, 0, 32, vcc
	v_ldexp_f32 v7, v7, v8
	v_log_f32_e32 v7, v7
	v_min_f32_e32 v4, 0, v6
	v_add_f32_e32 v6, v90, v15
	v_mul_f32_e64 v8, |v6|, s93
	v_exp_f32_e32 v8, v8
	v_mul_f32_e32 v5, 0x3f317217, v7
	v_fma_f32 v5, v7, s95, -v5
	v_fmac_f32_e32 v5, 0x3377d1cf, v7
	v_fmac_f32_e32 v5, 0x3f317217, v7
	v_cmp_lt_f32_e64 s[0:1], |v7|, s96
	v_add_f32_e32 v8, 1.0, v8
	v_lshlrev_b32_e32 v46, 16, v54
	v_cndmask_b32_e64 v5, v7, v5, s[0:1]
	v_cndmask_b32_e32 v7, 0, v231, vcc
	v_cmp_gt_f32_e32 vcc, s94, v8
	v_sub_f32_e32 v5, v5, v7
	v_sub_f32_e32 v38, v4, v5
	v_cndmask_b32_e64 v9, 0, 32, vcc
	v_ldexp_f32 v8, v8, v9
	v_log_f32_e32 v8, v8
	v_min_f32_e32 v4, 0, v6
	v_add_f32_e32 v6, v90, v16
	v_mul_f32_e64 v7, |v6|, s93
	v_exp_f32_e32 v7, v7
	v_mul_f32_e32 v5, 0x3f317217, v8
	v_fma_f32 v5, v8, s95, -v5
	v_fmac_f32_e32 v5, 0x3377d1cf, v8
	v_fmac_f32_e32 v5, 0x3f317217, v8
	v_cmp_lt_f32_e64 s[0:1], |v8|, s96
	v_add_f32_e32 v7, 1.0, v7
	v_and_b32_e32 v47, 0xffff0000, v54
	v_cndmask_b32_e64 v5, v8, v5, s[0:1]
	v_cndmask_b32_e32 v8, 0, v231, vcc
	v_cmp_gt_f32_e32 vcc, s94, v7
	v_sub_f32_e32 v5, v5, v8
	v_sub_f32_e32 v39, v4, v5
	v_cndmask_b32_e64 v8, 0, 32, vcc
	v_ldexp_f32 v7, v7, v8
	v_log_f32_e32 v7, v7
	v_min_f32_e32 v4, 0, v6
	v_add_f32_e32 v6, v90, v17
	v_mul_f32_e64 v8, |v6|, s93
	v_exp_f32_e32 v8, v8
	v_mul_f32_e32 v5, 0x3f317217, v7
	v_fma_f32 v5, v7, s95, -v5
	v_fmac_f32_e32 v5, 0x3377d1cf, v7
	v_fmac_f32_e32 v5, 0x3f317217, v7
	v_cmp_lt_f32_e64 s[0:1], |v7|, s96
	v_add_f32_e32 v8, 1.0, v8
	v_pk_add_f32 v[46:47], v[48:49], v[46:47] neg_lo:[0,1] neg_hi:[0,1]
	v_cndmask_b32_e64 v5, v7, v5, s[0:1]
	v_cndmask_b32_e32 v7, 0, v231, vcc
	v_cmp_gt_f32_e32 vcc, s94, v8
	v_sub_f32_e32 v5, v5, v7
	v_sub_f32_e32 v40, v4, v5
	v_cndmask_b32_e64 v9, 0, 32, vcc
	v_ldexp_f32 v8, v8, v9
	v_log_f32_e32 v8, v8
	v_min_f32_e32 v4, 0, v6
	v_cndmask_b32_e32 v6, 0, v231, vcc
	v_lshlrev_b32_e32 v48, 16, v55
	v_mul_f32_e32 v5, 0x3f317217, v8
	v_fma_f32 v5, v8, s95, -v5
	v_fmac_f32_e32 v5, 0x3377d1cf, v8
	v_fmac_f32_e32 v5, 0x3f317217, v8
	v_cmp_lt_f32_e64 s[0:1], |v8|, s96
	v_and_b32_e32 v49, 0xffff0000, v55
	v_cvt_pk_bf16_f32 v46, v46, v47
	v_cndmask_b32_e64 v5, v8, v5, s[0:1]
	v_sub_f32_e32 v5, v5, v6
	v_sub_f32_e32 v41, v4, v5
	v_mfma_f32_32x32x16_bf16 v[2:17], v[52:55], v[18:21], 0
	v_mul_f32_e32 v43, 0x3d800000, v31
	v_mul_f32_e32 v58, 0x3d800000, v33
	v_fmac_f32_e32 v43, 0x3d800000, v30
	v_fmac_f32_e32 v58, 0x3d800000, v32
	v_mul_f32_e32 v59, 0x3d800000, v35
	v_mul_f32_e32 v60, 0x3d800000, v37
	v_fmac_f32_e32 v59, 0x3d800000, v34
	v_mfma_f32_32x32x16_bf16 v[2:17], v[52:55], v[22:25], v[2:17]
	v_add_f32_e64 v22, v50, -v48
	v_add_f32_e64 v23, v51, -v49
	v_fmac_f32_e32 v60, 0x3d800000, v36
	v_cvt_pk_bf16_f32 v47, v22, v23
	v_add_f32_e32 v22, v43, v58
	v_mul_f32_e32 v61, 0x3d800000, v39
	v_mul_f32_e32 v62, 0x3d800000, v41
	v_fmac_f32_e32 v61, 0x3d800000, v38
	v_mfma_f32_32x32x16_bf16 v[2:17], v[44:47], v[18:21], v[2:17]
	v_add_f32_e32 v19, v59, v60
	v_fmac_f32_e32 v62, 0x3d800000, v40
	v_add_f32_e32 v21, v61, v62
	s_nop 8
	v_add_f32_e32 v2, v90, v2
	v_mul_f32_e64 v18, |v2|, s93
	v_exp_f32_e32 v18, v18
	v_add_f32_e32 v3, v90, v3
	v_mul_f32_e64 v23, |v3|, s93
	v_exp_f32_e32 v23, v23
	v_add_f32_e32 v18, 1.0, v18
	v_cmp_gt_f32_e32 vcc, s94, v18
	v_add_f32_e32 v4, v90, v4
	v_add_f32_e32 v23, 1.0, v23
	v_cndmask_b32_e64 v20, 0, 32, vcc
	v_ldexp_f32 v18, v18, v20
	v_log_f32_e32 v18, v18
	v_min_f32_e32 v2, 0, v2
	v_add_f32_e32 v5, v90, v5
	v_add_f32_e32 v6, v90, v6
	v_mul_f32_e32 v20, 0x3f317217, v18
	v_fma_f32 v20, v18, s95, -v20
	v_fmac_f32_e32 v20, 0x3377d1cf, v18
	v_fmac_f32_e32 v20, 0x3f317217, v18
	v_cmp_lt_f32_e64 s[0:1], |v18|, s96
	v_add_f32_e32 v7, v90, v7
	v_add_f32_e32 v8, v90, v8
	v_cndmask_b32_e64 v18, v18, v20, s[0:1]
	v_cndmask_b32_e32 v20, 0, v231, vcc
	v_cmp_gt_f32_e32 vcc, s94, v23
	v_sub_f32_e32 v18, v18, v20
	v_mul_f32_e64 v20, |v4|, s93
	v_cndmask_b32_e64 v24, 0, 32, vcc
	v_ldexp_f32 v23, v23, v24
	v_log_f32_e32 v23, v23
	v_exp_f32_e32 v20, v20
	v_sub_f32_e32 v2, v2, v18
	v_mul_f32_e64 v24, |v5|, s93
	v_mul_f32_e32 v18, 0x3f317217, v23
	v_fma_f32 v18, v23, s95, -v18
	v_fmac_f32_e32 v18, 0x3377d1cf, v23
	v_fmac_f32_e32 v18, 0x3f317217, v23
	v_cmp_lt_f32_e64 s[0:1], |v23|, s96
	v_add_f32_e32 v20, 1.0, v20
	v_exp_f32_e32 v24, v24
	v_cndmask_b32_e64 v18, v23, v18, s[0:1]
	v_cndmask_b32_e32 v23, 0, v231, vcc
	v_cmp_gt_f32_e32 vcc, s94, v20
	v_sub_f32_e32 v18, v18, v23
	v_add_f32_e32 v24, 1.0, v24
	v_cndmask_b32_e64 v23, 0, 32, vcc
	v_ldexp_f32 v20, v20, v23
	v_log_f32_e32 v20, v20
	v_min_f32_e32 v4, 0, v4
	v_add_f32_e32 v9, v90, v9
	v_add_f32_e32 v10, v90, v10
	v_mul_f32_e32 v23, 0x3f317217, v20
	v_fma_f32 v23, v20, s95, -v23
	v_fmac_f32_e32 v23, 0x3377d1cf, v20
	v_fmac_f32_e32 v23, 0x3f317217, v20
	v_cmp_lt_f32_e64 s[0:1], |v20|, s96
	v_add_f32_e32 v11, v90, v11
	v_add_f32_e32 v12, v90, v12
	v_cndmask_b32_e64 v20, v20, v23, s[0:1]
	v_cndmask_b32_e32 v23, 0, v231, vcc
	v_cmp_gt_f32_e32 vcc, s94, v24
	v_sub_f32_e32 v20, v20, v23
	v_mul_f32_e64 v23, |v6|, s93
	v_cndmask_b32_e64 v25, 0, 32, vcc
	v_ldexp_f32 v24, v24, v25
	v_log_f32_e32 v24, v24
	v_exp_f32_e32 v23, v23
	v_sub_f32_e32 v4, v4, v20
	v_mul_f32_e64 v25, |v7|, s93
	v_mul_f32_e32 v20, 0x3f317217, v24
	v_fma_f32 v20, v24, s95, -v20
	v_fmac_f32_e32 v20, 0x3377d1cf, v24
	v_fmac_f32_e32 v20, 0x3f317217, v24
	v_cmp_lt_f32_e64 s[0:1], |v24|, s96
	v_add_f32_e32 v23, 1.0, v23
	v_exp_f32_e32 v25, v25
	v_cndmask_b32_e64 v20, v24, v20, s[0:1]
	v_cndmask_b32_e32 v24, 0, v231, vcc
	v_cmp_gt_f32_e32 vcc, s94, v23
	v_sub_f32_e32 v20, v20, v24
	v_add_f32_e32 v25, 1.0, v25
	v_cndmask_b32_e64 v24, 0, 32, vcc
	v_ldexp_f32 v23, v23, v24
	v_log_f32_e32 v23, v23
	v_min_f32_e32 v6, 0, v6
	v_add_f32_e32 v13, v90, v13
	v_add_f32_e32 v15, v90, v15
	v_mul_f32_e32 v24, 0x3f317217, v23
	v_fma_f32 v24, v23, s95, -v24
	v_fmac_f32_e32 v24, 0x3377d1cf, v23
	v_fmac_f32_e32 v24, 0x3f317217, v23
	v_cmp_lt_f32_e64 s[0:1], |v23|, s96
	v_min_f32_e32 v7, 0, v7
	v_min_f32_e32 v3, 0, v3
	v_cndmask_b32_e64 v23, v23, v24, s[0:1]
	v_cndmask_b32_e32 v24, 0, v231, vcc
	v_cmp_gt_f32_e32 vcc, s94, v25
	v_sub_f32_e32 v23, v23, v24
	v_mul_f32_e64 v24, |v8|, s93
	v_cndmask_b32_e64 v43, 0, 32, vcc
	v_ldexp_f32 v25, v25, v43
	v_log_f32_e32 v25, v25
	v_exp_f32_e32 v24, v24
	v_sub_f32_e32 v6, v6, v23
	v_mul_f32_e64 v43, |v9|, s93
	v_mul_f32_e32 v23, 0x3f317217, v25
	v_fma_f32 v23, v25, s95, -v23
	v_fmac_f32_e32 v23, 0x3377d1cf, v25
	v_fmac_f32_e32 v23, 0x3f317217, v25
	v_cmp_lt_f32_e64 s[0:1], |v25|, s96
	v_add_f32_e32 v24, 1.0, v24
	v_exp_f32_e32 v43, v43
	v_cndmask_b32_e64 v23, v25, v23, s[0:1]
	v_cndmask_b32_e32 v25, 0, v231, vcc
	v_cmp_gt_f32_e32 vcc, s94, v24
	v_sub_f32_e32 v23, v23, v25
	v_add_f32_e32 v43, 1.0, v43
	v_cndmask_b32_e64 v25, 0, 32, vcc
	v_ldexp_f32 v24, v24, v25
	v_log_f32_e32 v24, v24
	v_min_f32_e32 v8, 0, v8
	v_min_f32_e32 v9, 0, v9
	v_sub_f32_e32 v7, v7, v23
	v_mul_f32_e32 v25, 0x3f317217, v24
	v_fma_f32 v25, v24, s95, -v25
	v_fmac_f32_e32 v25, 0x3377d1cf, v24
	v_fmac_f32_e32 v25, 0x3f317217, v24
	v_cmp_lt_f32_e64 s[0:1], |v24|, s96
	v_mul_f32_e32 v23, 0x3d800000, v7
	v_fmac_f32_e32 v23, 0x3d800000, v6
	v_cndmask_b32_e64 v24, v24, v25, s[0:1]
	v_cndmask_b32_e32 v25, 0, v231, vcc
	v_cmp_gt_f32_e32 vcc, s94, v43
	v_sub_f32_e32 v24, v24, v25
	v_mul_f32_e64 v25, |v10|, s93
	v_cndmask_b32_e64 v44, 0, 32, vcc
	v_ldexp_f32 v43, v43, v44
	v_log_f32_e32 v43, v43
	v_exp_f32_e32 v25, v25
	v_sub_f32_e32 v8, v8, v24
	v_mul_f32_e64 v44, |v11|, s93
	v_mul_f32_e32 v24, 0x3f317217, v43
	v_fma_f32 v24, v43, s95, -v24
	v_fmac_f32_e32 v24, 0x3377d1cf, v43
	v_fmac_f32_e32 v24, 0x3f317217, v43
	v_cmp_lt_f32_e64 s[0:1], |v43|, s96
	v_add_f32_e32 v25, 1.0, v25
	v_exp_f32_e32 v44, v44
	v_cndmask_b32_e64 v24, v43, v24, s[0:1]
	v_cndmask_b32_e32 v43, 0, v231, vcc
	v_cmp_gt_f32_e32 vcc, s94, v25
	v_sub_f32_e32 v24, v24, v43
	v_add_f32_e32 v44, 1.0, v44
	v_cndmask_b32_e64 v43, 0, 32, vcc
	v_ldexp_f32 v25, v25, v43
	v_log_f32_e32 v25, v25
	v_min_f32_e32 v10, 0, v10
	v_sub_f32_e32 v9, v9, v24
	v_mul_f32_e32 v24, 0x3d800000, v9
	v_mul_f32_e32 v43, 0x3f317217, v25
	v_fma_f32 v43, v25, s95, -v43
	v_fmac_f32_e32 v43, 0x3377d1cf, v25
	v_fmac_f32_e32 v43, 0x3f317217, v25
	v_cmp_lt_f32_e64 s[0:1], |v25|, s96
	v_fmac_f32_e32 v24, 0x3d800000, v8
	v_add_f32_e32 v23, v23, v24
	v_cndmask_b32_e64 v25, v25, v43, s[0:1]
	v_cndmask_b32_e32 v43, 0, v231, vcc
	v_cmp_gt_f32_e32 vcc, s94, v44
	v_sub_f32_e32 v25, v25, v43
	v_mul_f32_e64 v43, |v12|, s93
	v_cndmask_b32_e64 v45, 0, 32, vcc
	v_ldexp_f32 v44, v44, v45
	v_log_f32_e32 v44, v44
	v_exp_f32_e32 v43, v43
	v_sub_f32_e32 v25, v10, v25
	v_min_f32_e32 v10, 0, v11
	v_mul_f32_e32 v11, 0x3f317217, v44
	v_fma_f32 v11, v44, s95, -v11
	v_fmac_f32_e32 v11, 0x3377d1cf, v44
	v_fmac_f32_e32 v11, 0x3f317217, v44
	v_cmp_lt_f32_e64 s[0:1], |v44|, s96
	v_add_f32_e32 v43, 1.0, v43
	v_mul_f32_e64 v45, |v13|, s93
	v_cndmask_b32_e64 v11, v44, v11, s[0:1]
	v_cndmask_b32_e32 v44, 0, v231, vcc
	v_cmp_gt_f32_e32 vcc, s94, v43
	v_sub_f32_e32 v11, v11, v44
	v_exp_f32_e32 v45, v45
	v_cndmask_b32_e64 v44, 0, 32, vcc
	v_ldexp_f32 v43, v43, v44
	v_log_f32_e32 v43, v43
	v_sub_f32_e32 v44, v10, v11
	v_min_f32_e32 v11, 0, v12
	v_add_f32_e32 v45, 1.0, v45
	v_mul_f32_e32 v12, 0x3f317217, v43
	v_fma_f32 v12, v43, s95, -v12
	v_fmac_f32_e32 v12, 0x3377d1cf, v43
	v_fmac_f32_e32 v12, 0x3f317217, v43
	v_cmp_lt_f32_e64 s[0:1], |v43|, s96
	v_mul_f32_e32 v10, 0x3d800000, v44
	v_fmac_f32_e32 v10, 0x3d800000, v25
	v_cndmask_b32_e64 v12, v43, v12, s[0:1]
	v_cndmask_b32_e32 v43, 0, v231, vcc
	v_cmp_gt_f32_e32 vcc, s94, v45
	v_sub_f32_e32 v12, v12, v43
	v_sub_f32_e32 v43, v11, v12
	v_cndmask_b32_e64 v46, 0, 32, vcc
	v_ldexp_f32 v45, v45, v46
	v_log_f32_e32 v45, v45
	v_min_f32_e32 v11, 0, v13
	v_add_f32_e32 v13, v90, v14
	v_mul_f32_e64 v14, |v13|, s93
	v_exp_f32_e32 v14, v14
	v_mul_f32_e32 v12, 0x3f317217, v45
	v_fma_f32 v12, v45, s95, -v12
	v_fmac_f32_e32 v12, 0x3377d1cf, v45
	v_fmac_f32_e32 v12, 0x3f317217, v45
	v_cmp_lt_f32_e64 s[0:1], |v45|, s96
	v_add_f32_e32 v14, 1.0, v14
	v_mul_f32_e64 v46, |v15|, s93
	v_cndmask_b32_e64 v12, v45, v12, s[0:1]
	v_cndmask_b32_e32 v45, 0, v231, vcc
	v_cmp_gt_f32_e32 vcc, s94, v14
	v_sub_f32_e32 v12, v12, v45
	v_exp_f32_e32 v46, v46
	v_cndmask_b32_e64 v45, 0, 32, vcc
	v_ldexp_f32 v14, v14, v45
	v_log_f32_e32 v14, v14
	v_sub_f32_e32 v45, v11, v12
	v_min_f32_e32 v12, 0, v13
	v_add_f32_e32 v46, 1.0, v46
	v_mul_f32_e32 v13, 0x3f317217, v14
	v_fma_f32 v13, v14, s95, -v13
	v_fmac_f32_e32 v13, 0x3377d1cf, v14
	v_fmac_f32_e32 v13, 0x3f317217, v14
	v_cmp_lt_f32_e64 s[0:1], |v14|, s96
	v_mul_f32_e32 v11, 0x3d800000, v45
	v_fmac_f32_e32 v11, 0x3d800000, v43
	v_cndmask_b32_e64 v13, v14, v13, s[0:1]
	v_cndmask_b32_e32 v14, 0, v231, vcc
	v_cmp_gt_f32_e32 vcc, s94, v46
	v_sub_f32_e32 v13, v13, v14
	v_add_f32_e32 v14, v90, v16
	v_cndmask_b32_e64 v47, 0, 32, vcc
	v_ldexp_f32 v46, v46, v47
	v_log_f32_e32 v46, v46
	v_sub_f32_e32 v47, v12, v13
	v_min_f32_e32 v12, 0, v15
	v_mul_f32_e64 v15, |v14|, s93
	v_exp_f32_e32 v15, v15
	v_mul_f32_e32 v13, 0x3f317217, v46
	v_fma_f32 v13, v46, s95, -v13
	v_fmac_f32_e32 v13, 0x3377d1cf, v46
	v_fmac_f32_e32 v13, 0x3f317217, v46
	v_cmp_lt_f32_e64 s[0:1], |v46|, s96
	v_add_f32_e32 v15, 1.0, v15
	v_cndmask_b32_e32 v16, 0, v231, vcc
	v_cndmask_b32_e64 v13, v46, v13, s[0:1]
	v_cmp_gt_f32_e32 vcc, s94, v15
	v_sub_f32_e32 v13, v13, v16
	v_sub_f32_e32 v46, v12, v13
	v_cndmask_b32_e64 v16, 0, 32, vcc
	v_ldexp_f32 v15, v15, v16
	v_log_f32_e32 v15, v15
	v_add_f32_e32 v16, v90, v17
	v_mul_f32_e64 v17, |v16|, s93
	v_exp_f32_e32 v17, v17
	v_min_f32_e32 v13, 0, v14
	v_mul_f32_e32 v14, 0x3f317217, v15
	v_fma_f32 v14, v15, s95, -v14
	v_fmac_f32_e32 v14, 0x3377d1cf, v15
	v_fmac_f32_e32 v14, 0x3f317217, v15
	v_cmp_lt_f32_e64 s[0:1], |v15|, s96
	v_add_f32_e32 v17, 1.0, v17
	v_add_f32_e32 v24, v10, v11
	v_cndmask_b32_e64 v14, v15, v14, s[0:1]
	v_cndmask_b32_e32 v15, 0, v231, vcc
	v_cmp_gt_f32_e32 vcc, s94, v17
	v_sub_f32_e32 v14, v14, v15
	v_mul_f32_e32 v12, 0x3d800000, v46
	v_cndmask_b32_e64 v48, 0, 32, vcc
	v_ldexp_f32 v17, v17, v48
	v_log_f32_e32 v17, v17
	v_sub_f32_e32 v48, v13, v14
	v_cndmask_b32_e32 v15, 0, v231, vcc
	v_min_f32_e32 v13, 0, v16
	v_mul_f32_e32 v14, 0x3f317217, v17
	v_fma_f32 v14, v17, s95, -v14
	v_fmac_f32_e32 v14, 0x3377d1cf, v17
	v_fmac_f32_e32 v14, 0x3f317217, v17
	v_cmp_lt_f32_e64 s[0:1], |v17|, s96
	v_fmac_f32_e32 v12, 0x3d800000, v47
	v_min_f32_e32 v5, 0, v5
	v_cndmask_b32_e64 v14, v17, v14, s[0:1]
	v_sub_f32_e32 v14, v14, v15
	v_sub_f32_e32 v49, v13, v14
	ds_bpermute_b32 v14, v1, v42
	v_mul_f32_e32 v13, 0x3d800000, v49
	v_fmac_f32_e32 v13, 0x3d800000, v48
	v_add_f32_e32 v51, v12, v13
	v_sub_f32_e32 v3, v3, v18
	s_waitcnt lgkmcnt(0)
	v_add_f32_e32 v10, 0, v14
	v_cndmask_b32_e64 v52, v10, 0, s[4:5]
	ds_bpermute_b32 v10, v1, v22
	v_fmac_f32_e32 v52, 0x3d800000, v26
	v_fmamk_f32 v26, v27, 0x3d800000, v52
	v_add_f32_e32 v11, v42, v14
	v_fmamk_f32 v27, v28, 0x3d800000, v26
	v_add_f32_e32 v11, 0, v11
	s_waitcnt lgkmcnt(0)
	v_cndmask_b32_e64 v12, v10, 0, s[4:5]
	v_fmamk_f32 v28, v29, 0x3d800000, v27
	v_add_f32_e32 v29, v12, v11
	ds_bpermute_b32 v12, v1, v19
	v_add_f32_e32 v10, v22, v10
	v_add_f32_e32 v10, v10, v11
	v_sub_f32_e32 v5, v5, v20
	v_fmac_f32_e32 v29, 0x3d800000, v30
	s_waitcnt lgkmcnt(0)
	v_cndmask_b32_e64 v11, v12, 0, s[4:5]
	v_add_f32_e32 v22, v11, v10
	ds_bpermute_b32 v11, v1, v21
	v_mul_f32_e32 v18, 0x3d800000, v3
	v_mul_f32_e32 v20, 0x3d800000, v5
	v_fmamk_f32 v30, v31, 0x3d800000, v29
	v_fmac_f32_e32 v18, 0x3d800000, v2
	v_fmac_f32_e32 v20, 0x3d800000, v4
	v_fmamk_f32 v31, v32, 0x3d800000, v30
	v_fmac_f32_e32 v22, 0x3d800000, v34
	v_add_f32_e32 v12, v19, v12
	v_add_f32_e32 v50, v18, v20
	v_fmamk_f32 v32, v33, 0x3d800000, v31
	v_fmamk_f32 v33, v35, 0x3d800000, v22
	v_add_f32_e32 v10, v12, v10
	s_waitcnt lgkmcnt(0)
	v_cndmask_b32_e64 v12, v11, 0, s[4:5]
	v_fmamk_f32 v34, v36, 0x3d800000, v33
	v_add_f32_e32 v36, v12, v10
	ds_bpermute_b32 v12, v1, v50
	v_add_f32_e32 v11, v21, v11
	v_add_f32_e32 v10, v11, v10
	v_fmac_f32_e32 v36, 0x3d800000, v38
	v_mul_f32_e32 v21, 0x3fb8aa3b, v52
	s_waitcnt lgkmcnt(0)
	v_cndmask_b32_e64 v11, v12, 0, s[4:5]
	v_add_f32_e32 v17, v11, v10
	v_fmac_f32_e32 v17, 0x3d800000, v2
	ds_bpermute_b32 v2, v1, v23
	v_fmamk_f32 v16, v3, 0x3d800000, v17
	v_add_f32_e32 v3, v50, v12
	v_fmamk_f32 v15, v4, 0x3d800000, v16
	v_add_f32_e32 v3, v10, v3
	s_waitcnt lgkmcnt(0)
	v_cndmask_b32_e64 v4, v2, 0, s[4:5]
	v_add_f32_e32 v13, v4, v3
	ds_bpermute_b32 v4, v1, v24
	v_fmac_f32_e32 v13, 0x3d800000, v6
	v_fmamk_f32 v12, v7, 0x3d800000, v13
	v_add_f32_e32 v2, v23, v2
	v_fmamk_f32 v11, v8, 0x3d800000, v12
	v_add_f32_e32 v2, v2, v3
	s_waitcnt lgkmcnt(0)
	v_cndmask_b32_e64 v3, v4, 0, s[4:5]
	v_fmamk_f32 v10, v9, 0x3d800000, v11
	v_add_f32_e32 v9, v3, v2
	ds_bpermute_b32 v3, v1, v51
	v_fmamk_f32 v20, v39, 0x3d800000, v36
	v_exp_f32_e32 v21, v21
	v_fmamk_f32 v19, v40, 0x3d800000, v20
	v_add_f32_e32 v4, v24, v4
	v_fmamk_f32 v35, v37, 0x3d800000, v34
	v_fmamk_f32 v18, v41, 0x3d800000, v19
	v_fmac_f32_e32 v9, 0x3d800000, v25
	v_add_f32_e32 v2, v4, v2
	s_waitcnt lgkmcnt(0)
	v_cndmask_b32_e64 v3, v3, 0, s[4:5]
	ds_read_u16 v23, v188 offset:6144
	ds_read_u16 v24, v188 offset:6288
	ds_read_u16 v25, v188 offset:6432
	ds_read_u16 v37, v188 offset:6576
	ds_read_u16 v38, v188 offset:7296
	ds_read_u16 v39, v188 offset:7440
	ds_read_u16 v40, v188 offset:7584
	ds_read_u16 v41, v188 offset:7728
	v_fmamk_f32 v14, v5, 0x3d800000, v15
	v_add_f32_e32 v5, v3, v2
	s_waitcnt lgkmcnt(7)
	v_lshlrev_b32_e32 v23, 16, v23
	v_fmac_f32_e32 v5, 0x3d800000, v47
	v_mul_f32_e32 v21, v21, v23
	v_mul_f32_e32 v23, 0xbfb8aa3b, v52
	v_fmamk_f32 v8, v44, 0x3d800000, v9
	v_fmamk_f32 v4, v46, 0x3d800000, v5
	v_exp_f32_e32 v23, v23
	v_fmamk_f32 v7, v43, 0x3d800000, v8
	v_fmamk_f32 v3, v48, 0x3d800000, v4
	v_fmamk_f32 v6, v45, 0x3d800000, v7
	v_fmamk_f32 v2, v49, 0x3d800000, v3
	ds_read_u16 v42, v188 offset:43008
	ds_read_u16 v43, v188 offset:43152
	ds_read_u16 v44, v188 offset:43296
	ds_read_u16 v45, v188 offset:43440
	ds_read_u16 v46, v188 offset:44160
	ds_read_u16 v47, v188 offset:44304
	ds_read_u16 v48, v188 offset:44448
	ds_read_u16 v49, v188 offset:44592
	v_mul_f32_e32 v21, 0x3e000000, v21
	s_waitcnt lgkmcnt(7)
	v_lshlrev_b32_e32 v42, 16, v42
	v_mul_f32_e32 v23, v23, v42
	v_bfe_u32 v42, v21, 16, 1
	v_add3_u32 v21, v21, v42, s97
	ds_write_b16_d16_hi v188, v21 offset:6144
	v_bfe_u32 v21, v23, 16, 1
	v_add3_u32 v21, v23, v21, s97
	ds_write_b16_d16_hi v188, v21 offset:43008
	v_mul_f32_e32 v21, 0x3fb8aa3b, v26
	v_exp_f32_e32 v21, v21
	v_lshlrev_b32_e32 v23, 16, v24
	v_mul_f32_e32 v24, 0xbfb8aa3b, v26
	v_exp_f32_e32 v24, v24
	v_mul_f32_e32 v21, v21, v23
	v_mul_f32_e32 v21, 0x3e000000, v21
	s_waitcnt lgkmcnt(8)
	v_lshlrev_b32_e32 v23, 16, v43
	v_mul_f32_e32 v23, v24, v23
	v_bfe_u32 v24, v21, 16, 1
	v_add3_u32 v21, v21, v24, s97
	ds_write_b16_d16_hi v188, v21 offset:6288
	v_bfe_u32 v21, v23, 16, 1
	v_add3_u32 v21, v23, v21, s97
	ds_write_b16_d16_hi v188, v21 offset:43152
	v_mul_f32_e32 v21, 0x3fb8aa3b, v27
	v_exp_f32_e32 v21, v21
	v_mul_f32_e32 v24, 0xbfb8aa3b, v27
	v_exp_f32_e32 v24, v24
	v_lshlrev_b32_e32 v23, 16, v25
	v_mul_f32_e32 v21, v21, v23
	v_mul_f32_e32 v21, 0x3e000000, v21
	s_waitcnt lgkmcnt(9)
	v_lshlrev_b32_e32 v23, 16, v44
	v_mul_f32_e32 v23, v24, v23
	v_bfe_u32 v24, v21, 16, 1
	v_add3_u32 v21, v21, v24, s97
	ds_write_b16_d16_hi v188, v21 offset:6432
	v_bfe_u32 v21, v23, 16, 1
	v_add3_u32 v21, v23, v21, s97
	ds_write_b16_d16_hi v188, v21 offset:43296
	v_mul_f32_e32 v21, 0x3fb8aa3b, v28
	v_exp_f32_e32 v21, v21
	v_mul_f32_e32 v24, 0xbfb8aa3b, v28
	v_exp_f32_e32 v24, v24
	v_lshlrev_b32_e32 v23, 16, v37
	v_mul_f32_e32 v21, v21, v23
	v_mul_f32_e32 v21, 0x3e000000, v21
	s_waitcnt lgkmcnt(10)
	v_lshlrev_b32_e32 v23, 16, v45
	v_mul_f32_e32 v23, v24, v23
	v_bfe_u32 v24, v21, 16, 1
	v_add3_u32 v21, v21, v24, s97
	ds_write_b16_d16_hi v188, v21 offset:6576
	v_bfe_u32 v21, v23, 16, 1
	v_add3_u32 v21, v23, v21, s97
	ds_write_b16_d16_hi v188, v21 offset:43440
	v_mul_f32_e32 v21, 0x3fb8aa3b, v29
	v_exp_f32_e32 v21, v21
	v_mul_f32_e32 v24, 0xbfb8aa3b, v29
	v_exp_f32_e32 v24, v24
	v_lshlrev_b32_e32 v23, 16, v38
	v_mul_f32_e32 v21, v21, v23
	v_mul_f32_e32 v21, 0x3e000000, v21
	s_waitcnt lgkmcnt(11)
	v_lshlrev_b32_e32 v23, 16, v46
	v_mul_f32_e32 v23, v24, v23
	v_bfe_u32 v24, v21, 16, 1
	v_add3_u32 v21, v21, v24, s97
	ds_write_b16_d16_hi v188, v21 offset:7296
	v_bfe_u32 v21, v23, 16, 1
	v_add3_u32 v21, v23, v21, s97
	ds_write_b16_d16_hi v188, v21 offset:44160
	v_mul_f32_e32 v21, 0x3fb8aa3b, v30
	v_exp_f32_e32 v21, v21
	v_mul_f32_e32 v24, 0xbfb8aa3b, v30
	v_exp_f32_e32 v24, v24
	v_lshlrev_b32_e32 v23, 16, v39
	v_mul_f32_e32 v21, v21, v23
	v_mul_f32_e32 v21, 0x3e000000, v21
	s_waitcnt lgkmcnt(12)
	v_lshlrev_b32_e32 v23, 16, v47
	v_mul_f32_e32 v23, v24, v23
	v_bfe_u32 v24, v21, 16, 1
	v_add3_u32 v21, v21, v24, s97
	ds_write_b16_d16_hi v188, v21 offset:7440
	v_bfe_u32 v21, v23, 16, 1
	v_add3_u32 v21, v23, v21, s97
	ds_write_b16_d16_hi v188, v21 offset:44304
	v_mul_f32_e32 v21, 0x3fb8aa3b, v31
	v_exp_f32_e32 v21, v21
	v_mul_f32_e32 v24, 0xbfb8aa3b, v31
	v_exp_f32_e32 v24, v24
	v_lshlrev_b32_e32 v23, 16, v40
	v_mul_f32_e32 v21, v21, v23
	v_mul_f32_e32 v21, 0x3e000000, v21
	s_waitcnt lgkmcnt(13)
	v_lshlrev_b32_e32 v23, 16, v48
	v_mul_f32_e32 v23, v24, v23
	v_bfe_u32 v24, v21, 16, 1
	v_add3_u32 v21, v21, v24, s97
	ds_write_b16_d16_hi v188, v21 offset:7584
	v_bfe_u32 v21, v23, 16, 1
	v_add3_u32 v21, v23, v21, s97
	ds_write_b16_d16_hi v188, v21 offset:44448
	v_mul_f32_e32 v21, 0x3fb8aa3b, v32
	v_exp_f32_e32 v21, v21
	v_mul_f32_e32 v24, 0xbfb8aa3b, v32
	v_exp_f32_e32 v24, v24
	v_lshlrev_b32_e32 v23, 16, v41
	v_mul_f32_e32 v21, v21, v23
	v_mul_f32_e32 v21, 0x3e000000, v21
	s_waitcnt lgkmcnt(14)
	v_lshlrev_b32_e32 v23, 16, v49
	v_mul_f32_e32 v23, v24, v23
	v_bfe_u32 v24, v21, 16, 1
	v_add3_u32 v21, v21, v24, s97
	ds_write_b16_d16_hi v188, v21 offset:7728
	v_bfe_u32 v21, v23, 16, 1
	v_add3_u32 v21, v23, v21, s97
	ds_write_b16_d16_hi v188, v21 offset:44592
	v_mul_f32_e32 v21, 0x3fb8aa3b, v22
	v_exp_f32_e32 v21, v21
	v_mul_f32_e32 v22, 0xbfb8aa3b, v22
	ds_read_u16 v23, v188 offset:8448
	ds_read_u16 v24, v188 offset:8592
	ds_read_u16 v25, v188 offset:8736
	ds_read_u16 v26, v188 offset:8880
	ds_read_u16 v27, v188 offset:9600
	ds_read_u16 v28, v188 offset:9744
	ds_read_u16 v29, v188 offset:9888
	ds_read_u16 v30, v188 offset:10032
	v_exp_f32_e32 v22, v22
	s_waitcnt lgkmcnt(7)
	v_lshlrev_b32_e32 v23, 16, v23
	v_mul_f32_e32 v21, v21, v23
	ds_read_u16 v23, v188 offset:45312
	ds_read_u16 v31, v188 offset:45456
	ds_read_u16 v32, v188 offset:45600
	ds_read_u16 v37, v188 offset:45744
	ds_read_u16 v38, v188 offset:46464
	ds_read_u16 v39, v188 offset:46608
	ds_read_u16 v40, v188 offset:46752
	ds_read_u16 v41, v188 offset:46896
	v_mul_f32_e32 v21, 0x3e000000, v21
	s_waitcnt lgkmcnt(7)
	v_lshlrev_b32_e32 v23, 16, v23
	v_mul_f32_e32 v22, v22, v23
	v_bfe_u32 v23, v21, 16, 1
	v_add3_u32 v21, v21, v23, s97
	ds_write_b16_d16_hi v188, v21 offset:8448
	v_bfe_u32 v21, v22, 16, 1
	v_add3_u32 v21, v22, v21, s97
	ds_write_b16_d16_hi v188, v21 offset:45312
	v_mul_f32_e32 v21, 0x3fb8aa3b, v33
	v_exp_f32_e32 v21, v21
	v_mul_f32_e32 v23, 0xbfb8aa3b, v33
	v_exp_f32_e32 v23, v23
	v_lshlrev_b32_e32 v22, 16, v24
	v_mul_f32_e32 v21, v21, v22
	v_mul_f32_e32 v21, 0x3e000000, v21
	s_waitcnt lgkmcnt(8)
	v_lshlrev_b32_e32 v22, 16, v31
	v_mul_f32_e32 v22, v23, v22
	v_bfe_u32 v23, v21, 16, 1
	v_add3_u32 v21, v21, v23, s97
	ds_write_b16_d16_hi v188, v21 offset:8592
	v_bfe_u32 v21, v22, 16, 1
	v_add3_u32 v21, v22, v21, s97
	ds_write_b16_d16_hi v188, v21 offset:45456
	v_mul_f32_e32 v21, 0x3fb8aa3b, v34
	v_exp_f32_e32 v21, v21
	v_mul_f32_e32 v23, 0xbfb8aa3b, v34
	v_exp_f32_e32 v23, v23
	v_lshlrev_b32_e32 v22, 16, v25
	v_mul_f32_e32 v21, v21, v22
	v_mul_f32_e32 v21, 0x3e000000, v21
	s_waitcnt lgkmcnt(9)
	v_lshlrev_b32_e32 v22, 16, v32
	v_mul_f32_e32 v22, v23, v22
	v_bfe_u32 v23, v21, 16, 1
	v_add3_u32 v21, v21, v23, s97
	ds_write_b16_d16_hi v188, v21 offset:8736
	v_bfe_u32 v21, v22, 16, 1
	v_add3_u32 v21, v22, v21, s97
	ds_write_b16_d16_hi v188, v21 offset:45600
	v_mul_f32_e32 v21, 0x3fb8aa3b, v35
	v_exp_f32_e32 v21, v21
	v_mul_f32_e32 v23, 0xbfb8aa3b, v35
	v_exp_f32_e32 v23, v23
	v_lshlrev_b32_e32 v22, 16, v26
	v_mul_f32_e32 v21, v21, v22
	v_mul_f32_e32 v21, 0x3e000000, v21
	s_waitcnt lgkmcnt(10)
	v_lshlrev_b32_e32 v22, 16, v37
	v_mul_f32_e32 v22, v23, v22
	v_bfe_u32 v23, v21, 16, 1
	v_add3_u32 v21, v21, v23, s97
	ds_write_b16_d16_hi v188, v21 offset:8880
	v_bfe_u32 v21, v22, 16, 1
	v_add3_u32 v21, v22, v21, s97
	ds_write_b16_d16_hi v188, v21 offset:45744
	v_mul_f32_e32 v21, 0x3fb8aa3b, v36
	v_exp_f32_e32 v21, v21
	v_mul_f32_e32 v23, 0xbfb8aa3b, v36
	v_exp_f32_e32 v23, v23
	v_lshlrev_b32_e32 v22, 16, v27
	v_mul_f32_e32 v21, v21, v22
	v_mul_f32_e32 v21, 0x3e000000, v21
	s_waitcnt lgkmcnt(11)
	v_lshlrev_b32_e32 v22, 16, v38
	v_mul_f32_e32 v22, v23, v22
	v_bfe_u32 v23, v21, 16, 1
	v_add3_u32 v21, v21, v23, s97
	ds_write_b16_d16_hi v188, v21 offset:9600
	v_bfe_u32 v21, v22, 16, 1
	v_add3_u32 v21, v22, v21, s97
	ds_write_b16_d16_hi v188, v21 offset:46464
	v_mul_f32_e32 v21, 0x3fb8aa3b, v20
	v_exp_f32_e32 v21, v21
	v_mul_f32_e32 v20, 0xbfb8aa3b, v20
	v_exp_f32_e32 v20, v20
	v_lshlrev_b32_e32 v22, 16, v28
	v_mul_f32_e32 v21, v21, v22
	v_mul_f32_e32 v21, 0x3e000000, v21
	s_waitcnt lgkmcnt(12)
	v_lshlrev_b32_e32 v22, 16, v39
	v_mul_f32_e32 v20, v20, v22
	v_bfe_u32 v22, v21, 16, 1
	v_add3_u32 v21, v21, v22, s97
	ds_write_b16_d16_hi v188, v21 offset:9744
	v_bfe_u32 v21, v20, 16, 1
	v_add3_u32 v20, v20, v21, s97
	ds_write_b16_d16_hi v188, v20 offset:46608
	v_mul_f32_e32 v20, 0x3fb8aa3b, v19
	v_exp_f32_e32 v20, v20
	v_mul_f32_e32 v19, 0xbfb8aa3b, v19
	v_exp_f32_e32 v19, v19
	v_lshlrev_b32_e32 v21, 16, v29
	v_mul_f32_e32 v20, v20, v21
	v_mul_f32_e32 v20, 0x3e000000, v20
	s_waitcnt lgkmcnt(13)
	v_lshlrev_b32_e32 v21, 16, v40
	v_mul_f32_e32 v19, v19, v21
	v_bfe_u32 v21, v20, 16, 1
	v_add3_u32 v20, v20, v21, s97
	ds_write_b16_d16_hi v188, v20 offset:9888
	v_bfe_u32 v20, v19, 16, 1
	v_add3_u32 v19, v19, v20, s97
	ds_write_b16_d16_hi v188, v19 offset:46752
	v_mul_f32_e32 v19, 0x3fb8aa3b, v18
	v_exp_f32_e32 v19, v19
	v_mul_f32_e32 v18, 0xbfb8aa3b, v18
	v_exp_f32_e32 v18, v18
	v_lshlrev_b32_e32 v20, 16, v30
	v_mul_f32_e32 v19, v19, v20
	v_mul_f32_e32 v19, 0x3e000000, v19
	s_waitcnt lgkmcnt(14)
	v_lshlrev_b32_e32 v20, 16, v41
	v_mul_f32_e32 v18, v18, v20
	v_bfe_u32 v20, v19, 16, 1
	v_add3_u32 v19, v19, v20, s97
	ds_write_b16_d16_hi v188, v19 offset:10032
	v_bfe_u32 v19, v18, 16, 1
	v_add3_u32 v18, v18, v19, s97
	ds_write_b16_d16_hi v188, v18 offset:46896
	v_mul_f32_e32 v18, 0x3fb8aa3b, v17
	v_exp_f32_e32 v18, v18
	v_mul_f32_e32 v17, 0xbfb8aa3b, v17
	ds_read_u16 v19, v188 offset:10752
	ds_read_u16 v20, v188 offset:10896
	ds_read_u16 v21, v188 offset:11040
	ds_read_u16 v22, v188 offset:11184
	ds_read_u16 v23, v188 offset:11904
	ds_read_u16 v24, v188 offset:12048
	ds_read_u16 v25, v188 offset:12192
	ds_read_u16 v26, v188 offset:12336
	v_exp_f32_e32 v17, v17
	s_waitcnt lgkmcnt(7)
	v_lshlrev_b32_e32 v19, 16, v19
	v_mul_f32_e32 v18, v18, v19
	ds_read_u16 v19, v188 offset:47616
	ds_read_u16 v27, v188 offset:47760
	ds_read_u16 v28, v188 offset:47904
	ds_read_u16 v29, v188 offset:48048
	ds_read_u16 v30, v188 offset:48768
	ds_read_u16 v31, v188 offset:48912
	ds_read_u16 v32, v188 offset:49056
	ds_read_u16 v33, v188 offset:49200
	v_mul_f32_e32 v18, 0x3e000000, v18
	s_waitcnt lgkmcnt(7)
	v_lshlrev_b32_e32 v19, 16, v19
	v_mul_f32_e32 v17, v17, v19
	v_bfe_u32 v19, v18, 16, 1
	v_add3_u32 v18, v18, v19, s97
	ds_write_b16_d16_hi v188, v18 offset:10752
	v_bfe_u32 v18, v17, 16, 1
	v_add3_u32 v17, v17, v18, s97
	ds_write_b16_d16_hi v188, v17 offset:47616
	v_mul_f32_e32 v17, 0x3fb8aa3b, v16
	v_exp_f32_e32 v17, v17
	v_mul_f32_e32 v16, 0xbfb8aa3b, v16
	v_exp_f32_e32 v16, v16
	v_lshlrev_b32_e32 v18, 16, v20
	v_mul_f32_e32 v17, v17, v18
	v_mul_f32_e32 v17, 0x3e000000, v17
	s_waitcnt lgkmcnt(8)
	v_lshlrev_b32_e32 v18, 16, v27
	v_mul_f32_e32 v16, v16, v18
	v_bfe_u32 v18, v17, 16, 1
	v_add3_u32 v17, v17, v18, s97
	ds_write_b16_d16_hi v188, v17 offset:10896
	v_bfe_u32 v17, v16, 16, 1
	v_add3_u32 v16, v16, v17, s97
	ds_write_b16_d16_hi v188, v16 offset:47760
	v_mul_f32_e32 v16, 0x3fb8aa3b, v15
	v_exp_f32_e32 v16, v16
	v_mul_f32_e32 v15, 0xbfb8aa3b, v15
	v_exp_f32_e32 v15, v15
	v_lshlrev_b32_e32 v17, 16, v21
	v_mul_f32_e32 v16, v16, v17
	v_mul_f32_e32 v16, 0x3e000000, v16
	s_waitcnt lgkmcnt(9)
	v_lshlrev_b32_e32 v17, 16, v28
	v_mul_f32_e32 v15, v15, v17
	v_bfe_u32 v17, v16, 16, 1
	v_add3_u32 v16, v16, v17, s97
	ds_write_b16_d16_hi v188, v16 offset:11040
	v_bfe_u32 v16, v15, 16, 1
	v_add3_u32 v15, v15, v16, s97
	ds_write_b16_d16_hi v188, v15 offset:47904
	v_mul_f32_e32 v15, 0x3fb8aa3b, v14
	v_exp_f32_e32 v15, v15
	v_mul_f32_e32 v14, 0xbfb8aa3b, v14
	v_exp_f32_e32 v14, v14
	v_lshlrev_b32_e32 v16, 16, v22
	v_mul_f32_e32 v15, v15, v16
	v_mul_f32_e32 v15, 0x3e000000, v15
	s_waitcnt lgkmcnt(10)
	v_lshlrev_b32_e32 v16, 16, v29
	v_mul_f32_e32 v14, v14, v16
	v_bfe_u32 v16, v15, 16, 1
	v_add3_u32 v15, v15, v16, s97
	ds_write_b16_d16_hi v188, v15 offset:11184
	v_bfe_u32 v15, v14, 16, 1
	v_add3_u32 v14, v14, v15, s97
	ds_write_b16_d16_hi v188, v14 offset:48048
	v_mul_f32_e32 v14, 0x3fb8aa3b, v13
	v_exp_f32_e32 v14, v14
	v_mul_f32_e32 v13, 0xbfb8aa3b, v13
	v_exp_f32_e32 v13, v13
	v_lshlrev_b32_e32 v15, 16, v23
	v_mul_f32_e32 v14, v14, v15
	v_mul_f32_e32 v14, 0x3e000000, v14
	s_waitcnt lgkmcnt(11)
	v_lshlrev_b32_e32 v15, 16, v30
	v_mul_f32_e32 v13, v13, v15
	v_bfe_u32 v15, v14, 16, 1
	v_add3_u32 v14, v14, v15, s97
	ds_write_b16_d16_hi v188, v14 offset:11904
	v_bfe_u32 v14, v13, 16, 1
	v_add3_u32 v13, v13, v14, s97
	ds_write_b16_d16_hi v188, v13 offset:48768
	v_mul_f32_e32 v13, 0x3fb8aa3b, v12
	v_exp_f32_e32 v13, v13
	v_mul_f32_e32 v12, 0xbfb8aa3b, v12
	v_exp_f32_e32 v12, v12
	v_lshlrev_b32_e32 v14, 16, v24
	v_mul_f32_e32 v13, v13, v14
	v_mul_f32_e32 v13, 0x3e000000, v13
	s_waitcnt lgkmcnt(12)
	v_lshlrev_b32_e32 v14, 16, v31
	v_mul_f32_e32 v12, v12, v14
	v_bfe_u32 v14, v13, 16, 1
	v_add3_u32 v13, v13, v14, s97
	ds_write_b16_d16_hi v188, v13 offset:12048
	v_bfe_u32 v13, v12, 16, 1
	v_add3_u32 v12, v12, v13, s97
	ds_write_b16_d16_hi v188, v12 offset:48912
	v_mul_f32_e32 v12, 0x3fb8aa3b, v11
	v_exp_f32_e32 v12, v12
	v_mul_f32_e32 v11, 0xbfb8aa3b, v11
	v_exp_f32_e32 v11, v11
	v_lshlrev_b32_e32 v13, 16, v25
	v_mul_f32_e32 v12, v12, v13
	v_mul_f32_e32 v12, 0x3e000000, v12
	s_waitcnt lgkmcnt(13)
	v_lshlrev_b32_e32 v13, 16, v32
	v_mul_f32_e32 v11, v11, v13
	v_bfe_u32 v13, v12, 16, 1
	v_add3_u32 v12, v12, v13, s97
	ds_write_b16_d16_hi v188, v12 offset:12192
	v_bfe_u32 v12, v11, 16, 1
	v_add3_u32 v11, v11, v12, s97
	ds_write_b16_d16_hi v188, v11 offset:49056
	v_mul_f32_e32 v11, 0x3fb8aa3b, v10
	v_exp_f32_e32 v11, v11
	v_mul_f32_e32 v10, 0xbfb8aa3b, v10
	v_exp_f32_e32 v10, v10
	v_lshlrev_b32_e32 v12, 16, v26
	v_mul_f32_e32 v11, v11, v12
	v_mul_f32_e32 v11, 0x3e000000, v11
	s_waitcnt lgkmcnt(14)
	v_lshlrev_b32_e32 v12, 16, v33
	v_mul_f32_e32 v10, v10, v12
	v_bfe_u32 v12, v11, 16, 1
	v_add3_u32 v11, v11, v12, s97
	ds_write_b16_d16_hi v188, v11 offset:12336
	v_bfe_u32 v11, v10, 16, 1
	v_add3_u32 v10, v10, v11, s97
	ds_write_b16_d16_hi v188, v10 offset:49200
	v_mul_f32_e32 v10, 0x3fb8aa3b, v9
	v_exp_f32_e32 v10, v10
	v_mul_f32_e32 v9, 0xbfb8aa3b, v9
	ds_read_u16 v11, v188 offset:13056
	ds_read_u16 v12, v188 offset:13200
	ds_read_u16 v13, v188 offset:13344
	ds_read_u16 v14, v188 offset:13488
	ds_read_u16 v15, v188 offset:14208
	ds_read_u16 v16, v188 offset:14352
	ds_read_u16 v17, v188 offset:14496
	ds_read_u16 v28, v188 offset:14640
	v_exp_f32_e32 v9, v9
	s_waitcnt lgkmcnt(7)
	v_lshlrev_b32_e32 v11, 16, v11
	v_mul_f32_e32 v10, v10, v11
	ds_read_u16 v11, v188 offset:49920
	ds_read_u16 v18, v188 offset:50064
	ds_read_u16 v19, v188 offset:50208
	ds_read_u16 v20, v188 offset:50352
	ds_read_u16 v21, v188 offset:51072
	ds_read_u16 v22, v188 offset:51216
	ds_read_u16 v23, v188 offset:51360
	ds_read_u16 v29, v188 offset:51504
	v_mul_f32_e32 v10, 0x3e000000, v10
	s_waitcnt lgkmcnt(7)
	v_lshlrev_b32_e32 v11, 16, v11
	v_mul_f32_e32 v9, v9, v11
	v_bfe_u32 v11, v10, 16, 1
	v_add3_u32 v10, v10, v11, s97
	ds_write_b16_d16_hi v188, v10 offset:13056
	v_bfe_u32 v10, v9, 16, 1
	v_add3_u32 v9, v9, v10, s97
	ds_write_b16_d16_hi v188, v9 offset:49920
	v_mul_f32_e32 v9, 0x3fb8aa3b, v8
	v_exp_f32_e32 v9, v9
	v_mul_f32_e32 v8, 0xbfb8aa3b, v8
	v_exp_f32_e32 v8, v8
	v_lshlrev_b32_e32 v10, 16, v12
	v_mul_f32_e32 v9, v9, v10
	v_mul_f32_e32 v9, 0x3e000000, v9
	s_waitcnt lgkmcnt(8)
	v_lshlrev_b32_e32 v10, 16, v18
	v_mul_f32_e32 v8, v8, v10
	v_bfe_u32 v10, v9, 16, 1
	v_add3_u32 v9, v9, v10, s97
	ds_write_b16_d16_hi v188, v9 offset:13200
	v_bfe_u32 v9, v8, 16, 1
	v_add3_u32 v8, v8, v9, s97
	ds_write_b16_d16_hi v188, v8 offset:50064
	v_mul_f32_e32 v8, 0x3fb8aa3b, v7
	v_exp_f32_e32 v8, v8
	v_mul_f32_e32 v7, 0xbfb8aa3b, v7
	v_exp_f32_e32 v7, v7
	v_lshlrev_b32_e32 v9, 16, v13
	v_mul_f32_e32 v8, v8, v9
	v_mul_f32_e32 v8, 0x3e000000, v8
	s_waitcnt lgkmcnt(9)
	v_lshlrev_b32_e32 v9, 16, v19
	v_mul_f32_e32 v7, v7, v9
	v_bfe_u32 v9, v8, 16, 1
	v_add3_u32 v8, v8, v9, s97
	ds_write_b16_d16_hi v188, v8 offset:13344
	v_bfe_u32 v8, v7, 16, 1
	v_add3_u32 v7, v7, v8, s97
	ds_write_b16_d16_hi v188, v7 offset:50208
	v_mul_f32_e32 v7, 0x3fb8aa3b, v6
	v_exp_f32_e32 v7, v7
	v_mul_f32_e32 v6, 0xbfb8aa3b, v6
	v_exp_f32_e32 v6, v6
	v_lshlrev_b32_e32 v8, 16, v14
	v_mul_f32_e32 v7, v7, v8
	v_mul_f32_e32 v7, 0x3e000000, v7
	s_waitcnt lgkmcnt(10)
	v_lshlrev_b32_e32 v8, 16, v20
	v_mul_f32_e32 v6, v6, v8
	v_bfe_u32 v8, v7, 16, 1
	v_add3_u32 v7, v7, v8, s97
	ds_write_b16_d16_hi v188, v7 offset:13488
	v_bfe_u32 v7, v6, 16, 1
	v_add3_u32 v6, v6, v7, s97
	ds_write_b16_d16_hi v188, v6 offset:50352
	v_mul_f32_e32 v6, 0x3fb8aa3b, v5
	v_exp_f32_e32 v6, v6
	v_mul_f32_e32 v5, 0xbfb8aa3b, v5
	v_exp_f32_e32 v5, v5
	v_lshlrev_b32_e32 v7, 16, v15
	v_mul_f32_e32 v6, v6, v7
	v_mul_f32_e32 v6, 0x3e000000, v6
	s_waitcnt lgkmcnt(11)
	v_lshlrev_b32_e32 v7, 16, v21
	v_mul_f32_e32 v5, v5, v7
	v_bfe_u32 v7, v6, 16, 1
	v_add3_u32 v6, v6, v7, s97
	ds_write_b16_d16_hi v188, v6 offset:14208
	v_bfe_u32 v6, v5, 16, 1
	v_add3_u32 v5, v5, v6, s97
	ds_write_b16_d16_hi v188, v5 offset:51072
	v_mul_f32_e32 v5, 0x3fb8aa3b, v4
	v_exp_f32_e32 v9, v5
	v_mul_f32_e32 v4, 0xbfb8aa3b, v4
	v_exp_f32_e32 v10, v4
	v_lshlrev_b32_e32 v8, 16, v16
	v_mul_f32_e32 v8, v9, v8
	s_waitcnt lgkmcnt(12)
	v_lshlrev_b32_e32 v9, 16, v22
	s_lshl_b32 s0, s74, 2
	v_mul_f32_e32 v12, v10, v9
	s_add_i32 s0, s0, s49
	v_bfe_u32 v13, v12, 16, 1
	s_ashr_i32 s1, s0, 31
	v_add3_u32 v12, v12, v13, s97
	s_lshl_b64 s[0:1], s[0:1], 14
	ds_write_b16_d16_hi v188, v12 offset:51216
	v_mul_f32_e32 v12, 0x3fb8aa3b, v3
	v_lshl_add_u64 v[32:33], v[142:143], 0, s[0:1]
	v_lshlrev_b32_e32 v16, 16, v17
	v_exp_f32_e32 v17, v12
	global_load_dwordx4 v[4:7], v[32:33], off
	v_mul_f32_e32 v3, 0xbfb8aa3b, v3
	v_exp_f32_e32 v3, v3
	v_mul_f32_e32 v16, v17, v16
	v_mul_f32_e32 v16, 0x3e000000, v16
	s_waitcnt lgkmcnt(12)
	v_lshlrev_b32_e32 v17, 16, v23
	v_mul_f32_e32 v8, 0x3e000000, v8
	v_mul_f32_e32 v3, v3, v17
	v_bfe_u32 v17, v16, 16, 1
	s_movk_i32 s0, 0x2000
	v_bfe_u32 v9, v8, 16, 1
	v_add3_u32 v20, v16, v17, s97
	v_add_co_u32_e32 v34, vcc, s0, v32
	v_add3_u32 v8, v8, v9, s97
	ds_write_b16_d16_hi v188, v20 offset:14496
	v_bfe_u32 v20, v3, 16, 1
	v_addc_co_u32_e32 v35, vcc, 0, v33, vcc
	ds_write_b16_d16_hi v188, v8 offset:14352
	global_load_dwordx4 v[8:11], v[32:33], off offset:32
	v_add3_u32 v3, v3, v20, s97
	global_load_dwordx4 v[20:23], v[34:35], off offset:-4096
	v_add_co_u32_e32 v36, vcc, s83, v32
	global_load_dwordx4 v[12:15], v[32:33], off offset:64
	global_load_dwordx4 v[16:19], v[32:33], off offset:96
	v_addc_co_u32_e32 v37, vcc, 0, v33, vcc
	global_load_dwordx4 v[24:27], v[36:37], off offset:32
	ds_write_b16_d16_hi v188, v3 offset:51360
	v_mul_f32_e32 v3, 0x3fb8aa3b, v2
	v_exp_f32_e32 v3, v3
	v_mul_f32_e32 v2, 0xbfb8aa3b, v2
	v_exp_f32_e32 v2, v2
	v_lshlrev_b32_e32 v28, 16, v28
	v_mul_f32_e32 v3, v3, v28
	s_waitcnt lgkmcnt(14)
	v_lshlrev_b32_e32 v28, 16, v29
	v_mul_f32_e32 v2, v2, v28
	global_load_dwordx4 v[28:31], v[36:37], off offset:64
	v_mul_f32_e32 v3, 0x3e000000, v3
	v_bfe_u32 v38, v3, 16, 1
	v_add3_u32 v3, v3, v38, s97
	ds_write_b16_d16_hi v188, v3 offset:14640
	v_bfe_u32 v3, v2, 16, 1
	v_add3_u32 v2, v2, v3, s97
	ds_write_b16_d16_hi v188, v2 offset:51504
	global_load_dwordx4 v[66:69], v[36:37], off offset:96
	global_load_dwordx4 v[70:73], v[34:35], off
	global_load_dwordx4 v[232:235], v[34:35], off offset:32
	global_load_dwordx4 v[236:239], v[34:35], off offset:64
	global_load_dwordx4 v[240:243], v[34:35], off offset:96
	s_movk_i32 s0, 0x3000
	v_add_co_u32_e32 v2, vcc, s0, v32
	s_mov_b32 s0, 0
	s_nop 0
	v_addc_co_u32_e32 v3, vcc, 0, v33, vcc
	global_load_dwordx4 v[244:247], v[2:3], off
	global_load_dwordx4 v[248:251], v[2:3], off offset:32
	global_load_dwordx4 v[208:211], v[2:3], off offset:64
	global_load_dwordx4 v[212:215], v[2:3], off offset:96
	global_load_dwordx4 v[110:113], v[74:75], off offset:2048
	global_load_dwordx4 v[106:109], v[76:77], off offset:2048
	global_load_dwordx4 v[102:105], v[78:79], off offset:2048
	global_load_dwordx4 v[98:101], v[80:81], off offset:2048
	global_load_dwordx4 v[94:97], v[82:83], off offset:2048
	global_load_dwordx4 v[90:93], v[84:85], off offset:2048
	s_nop 0
	global_load_dwordx4 v[86:89], v[86:87], off offset:2048
	s_nop 0
	global_load_dwordx4 v[82:85], v[114:115], off offset:2048
	s_waitcnt lgkmcnt(0)
	s_barrier
	ds_read_b128 v[114:117], v206 offset:6144
	ds_read_b128 v[118:121], v206 offset:6176
	s_waitcnt vmcnt(23) lgkmcnt(1)
	v_mfma_f32_32x32x16_bf16 v[50:65], v[4:7], v[114:117], 0
	ds_read_b128 v[122:125], v206 offset:6208
	ds_read_b128 v[126:129], v206 offset:6240
	s_waitcnt vmcnt(22) lgkmcnt(2)
	v_mfma_f32_32x32x16_bf16 v[50:65], v[8:11], v[118:121], v[50:65]
	s_waitcnt vmcnt(21)
	v_mfma_f32_32x32x16_bf16 v[34:49], v[20:23], v[114:117], 0
	s_waitcnt vmcnt(20) lgkmcnt(1)
	v_mfma_f32_32x32x16_bf16 v[50:65], v[12:15], v[122:125], v[50:65]
	s_waitcnt vmcnt(18)
	v_mfma_f32_32x32x16_bf16 v[34:49], v[24:27], v[118:121], v[34:49]
	s_waitcnt lgkmcnt(0)
	v_mfma_f32_32x32x16_bf16 v[50:65], v[16:19], v[126:129], v[50:65]
	s_waitcnt vmcnt(17)
	v_mfma_f32_32x32x16_bf16 v[34:49], v[28:31], v[122:125], v[34:49]
	s_waitcnt vmcnt(15)
	v_mfma_f32_32x32x16_bf16 v[18:33], v[70:73], v[114:117], 0
	s_waitcnt vmcnt(11)
	v_mfma_f32_32x32x16_bf16 v[2:17], v[244:247], v[114:117], 0
	v_mfma_f32_32x32x16_bf16 v[18:33], v[232:235], v[118:121], v[18:33]
	v_mov_b32_e32 v232, v205
	s_waitcnt vmcnt(10)
	v_mfma_f32_32x32x16_bf16 v[2:17], v[248:251], v[118:121], v[2:17]
	v_mfma_f32_32x32x16_bf16 v[18:33], v[236:239], v[122:125], v[18:33]
	s_waitcnt vmcnt(9)
	v_mfma_f32_32x32x16_bf16 v[2:17], v[208:211], v[122:125], v[2:17]
	v_mfma_f32_32x32x16_bf16 v[34:49], v[66:69], v[126:129], v[34:49]
	v_mfma_f32_32x32x16_bf16 v[18:33], v[240:243], v[126:129], v[18:33]
	s_waitcnt vmcnt(8)
	v_mfma_f32_32x32x16_bf16 v[2:17], v[212:215], v[126:129], v[2:17]
	s_branch .LBB0_1422
